# S5: consumer waits only for its skip-input load (not the YS store acknowledgement); producer requests the u tile three chunks ahead into two register sets alternating by chunk parity
# speedup vs baseline: 1.0050x; 1.0050x over previous
; __device__ __forceinline__ unsigned pk2(float lo, float hi) { return f2bf(lo) | (f2bf(hi) << 16); }
; #define S5_SPIN(ptr, need) do { while ((int)(*(volatile LAS unsigned*)(ptr)) < (int)(need)) __builtin_amdgcn_s_sleep(1); } while (0)
; __device__ __forceinline__ void phase_s5p(const float* const (&in)[34], unsigned char* ws, LAS unsigned char* lds, int G) {
;     ...
;         } else {
;             bf16x8 cop[4];
; #pragma unroll
;             for (int ks = 0; ks < 4; ++ks) { const size_t o = (size_t)(g * 16 + fr) * 64 + ks * 16 + fq * 4;
;                 const f32x4 cr = *(const f32x4*)(in[26] + o), ci = *(const f32x4*)(in[27] + o);
;                 u32x4 w; w.x = pk2(cr[0], -ci[0]); w.y = pk2(cr[1], -ci[1]); w.z = pk2(cr[2], -ci[2]); w.w = pk2(cr[3], -ci[3]); cop[ks] = __builtin_bit_cast(bf16x8, w); }
;             const f32x4 dsk = *(const f32x4*)(in[28] + g * 16 + 4 * fq);
;             u32x2 uskn = *(const u32x2*)(U + (size_t)rowof(b, fr) * 2048 + g * 16 + 4 * fq);
; #pragma unroll 1
;             for (int ck = 0; ck < NCK; ++ck) {
;                 const u32x2 usk = uskn;
;                 { const int pc = ck + 1 < NCK ? ck + 1 : ck; uskn = *(const u32x2*)(U + (size_t)rowof(b, pc * 16 + fr) * 2048 + g * 16 + 4 * fq); }
;                 S5_SPIN(fprod, base + ck + 1);
.LBB0_1444:
	s_ashr_i32 s64, s3, 7
	s_and_b32 s65, s3, 0x7f
	s_andn2_b64 vcc, exec, s[10:11]
	s_mov_b64 s[4:5], -1
	s_cbranch_vccnz .LBB0_1452
	v_readlane_b32 s36, v227, 50
	v_lshl_or_b32 v3, s65, 12, v104
	v_readlane_b32 s42, v227, 56
	v_readlane_b32 s43, v227, 57
	v_readlane_b32 s40, v227, 54
	v_readlane_b32 s41, v227, 55
	s_nop 2
	global_load_dwordx4 v[8:11], v3, s[42:43]
	s_nop 0
	global_load_dwordx4 v[12:15], v3, s[40:41]
	global_load_dwordx4 v[16:19], v3, s[42:43] offset:64
	global_load_dwordx4 v[20:23], v3, s[40:41] offset:64
	global_load_dwordx4 v[24:27], v3, s[42:43] offset:128
	global_load_dwordx4 v[28:31], v3, s[40:41] offset:128
	global_load_dwordx4 v[34:37], v3, s[40:41] offset:192
	global_load_dwordx4 v[38:41], v3, s[42:43] offset:192
	s_lshl_b32 s14, s65, 6
	v_lshl_add_u64 v[4:5], v[90:91], 0, s[14:15]
	s_lshl_b32 s14, s65, 5
	v_lshl_add_u64 v[32:33], v[78:79], 0, s[14:15]
	global_load_dwordx4 v[4:7], v[4:5], off
	s_lshl_b32 s6, s64, 11
	global_load_dwordx2 v[32:33], v[32:33], off
	s_cmpk_lt_u32 s3, 0x80
	s_cselect_b64 s[4:5], -1, 0
	s_mov_b32 s8, 0
	s_xor_b64 s[4:5], s[4:5], -1
	v_readlane_b32 s37, v227, 51
	v_readlane_b32 s38, v227, 52
	v_readlane_b32 s39, v227, 53
	v_readlane_b32 s44, v227, 58
	v_readlane_b32 s45, v227, 59
	v_readlane_b32 s46, v227, 60
	v_readlane_b32 s47, v227, 61
	v_readlane_b32 s48, v227, 62
	v_readlane_b32 s49, v227, 63
	v_readlane_b32 s50, v226, 0
	v_readlane_b32 s51, v226, 1
	s_waitcnt vmcnt(9)
	v_xor_b32_e32 v3, 0x80000000, v11
	v_xor_b32_e32 v8, 0x80000000, v8
	v_xor_b32_e32 v9, 0x80000000, v9
	v_xor_b32_e32 v10, 0x80000000, v10
	s_waitcnt vmcnt(8)
	v_and_b32_sdwa v11, v13, v109 dst_sel:DWORD dst_unused:UNUSED_PAD src0_sel:WORD_1 src1_sel:DWORD
	v_and_b32_sdwa v42, v12, v109 dst_sel:DWORD dst_unused:UNUSED_PAD src0_sel:WORD_1 src1_sel:DWORD
	v_and_b32_sdwa v43, v15, v109 dst_sel:DWORD dst_unused:UNUSED_PAD src0_sel:WORD_1 src1_sel:DWORD
	v_and_b32_sdwa v44, v14, v109 dst_sel:DWORD dst_unused:UNUSED_PAD src0_sel:WORD_1 src1_sel:DWORD
	s_waitcnt vmcnt(7)
	v_xor_b32_e32 v16, 0x80000000, v16
	v_xor_b32_e32 v17, 0x80000000, v17
	s_waitcnt vmcnt(6)
	v_and_b32_sdwa v45, v21, v109 dst_sel:DWORD dst_unused:UNUSED_PAD src0_sel:WORD_1 src1_sel:DWORD
	v_and_b32_sdwa v46, v20, v109 dst_sel:DWORD dst_unused:UNUSED_PAD src0_sel:WORD_1 src1_sel:DWORD
	v_and_b32_sdwa v47, v23, v109 dst_sel:DWORD dst_unused:UNUSED_PAD src0_sel:WORD_1 src1_sel:DWORD
	v_xor_b32_e32 v19, 0x80000000, v19
	v_and_b32_sdwa v48, v22, v109 dst_sel:DWORD dst_unused:UNUSED_PAD src0_sel:WORD_1 src1_sel:DWORD
	v_add3_u32 v11, v13, v11, s21
	v_add3_u32 v12, v12, v42, s21
	v_add3_u32 v13, v15, v43, s21
	v_add3_u32 v14, v14, v44, s21
	v_bfe_u32 v15, v10, 16, 1
	v_bfe_u32 v42, v9, 16, 1
	v_bfe_u32 v43, v8, 16, 1
	v_bfe_u32 v44, v3, 16, 1
	v_add3_u32 v21, v21, v45, s21
	v_add3_u32 v20, v20, v46, s21
	v_add3_u32 v23, v23, v47, s21
	v_bfe_u32 v46, v17, 16, 1
	v_bfe_u32 v47, v16, 16, 1
	v_xor_b32_e32 v18, 0x80000000, v18
	s_waitcnt vmcnt(5)
	v_xor_b32_e32 v27, 0x80000000, v27
	v_xor_b32_e32 v24, 0x80000000, v24
	v_xor_b32_e32 v25, 0x80000000, v25
	v_xor_b32_e32 v26, 0x80000000, v26
	s_waitcnt vmcnt(4)
	v_and_b32_sdwa v49, v29, v109 dst_sel:DWORD dst_unused:UNUSED_PAD src0_sel:WORD_1 src1_sel:DWORD
	v_and_b32_sdwa v50, v28, v109 dst_sel:DWORD dst_unused:UNUSED_PAD src0_sel:WORD_1 src1_sel:DWORD
	v_and_b32_sdwa v52, v30, v109 dst_sel:DWORD dst_unused:UNUSED_PAD src0_sel:WORD_1 src1_sel:DWORD
	v_add3_u32 v22, v22, v48, s21
	v_bfe_u32 v48, v19, 16, 1
	v_lshrrev_b32_e32 v12, 16, v12
	v_lshrrev_b32_e32 v11, 16, v11
	v_add3_u32 v3, v3, v44, s21
	v_add3_u32 v8, v8, v43, s21
	v_add3_u32 v9, v9, v42, s21
	v_add3_u32 v10, v10, v15, s21
	v_lshrrev_b32_e32 v15, 16, v20
	v_lshrrev_b32_e32 v20, 16, v21
	v_add3_u32 v16, v16, v47, s21
	v_add3_u32 v17, v17, v46, s21
	v_bfe_u32 v45, v18, 16, 1
	v_add3_u32 v29, v29, v49, s21
	v_add3_u32 v28, v28, v50, s21
	v_add3_u32 v30, v30, v52, s21
	v_bfe_u32 v49, v26, 16, 1
	v_add3_u32 v19, v19, v48, s21
	v_and_or_b32 v9, v9, s28, v11
	v_and_or_b32 v8, v8, s28, v12
	v_perm_b32 v11, v3, v13, s29
	v_and_or_b32 v13, v17, s28, v20
	v_and_or_b32 v12, v16, s28, v15
	v_bfe_u32 v3, v25, 16, 1
	v_bfe_u32 v16, v24, 16, 1
	v_bfe_u32 v17, v27, 16, 1
	v_lshrrev_b32_e32 v14, 16, v14
	v_lshrrev_b32_e32 v21, 16, v22
	v_add3_u32 v18, v18, v45, s21
	v_lshrrev_b32_e32 v22, 16, v28
	v_lshrrev_b32_e32 v28, 16, v29
	v_lshrrev_b32_e32 v29, 16, v30
	v_perm_b32 v15, v19, v23, s29
	v_add3_u32 v19, v27, v17, s21
	v_add3_u32 v16, v24, v16, s21
	v_add3_u32 v3, v25, v3, s21
	v_add3_u32 v17, v26, v49, s21
	v_and_or_b32 v10, v10, s28, v14
	v_and_or_b32 v14, v18, s28, v21
	v_and_or_b32 v18, v17, s28, v29
	v_and_or_b32 v17, v3, s28, v28
	v_and_or_b32 v16, v16, s28, v22
	s_waitcnt vmcnt(2)
	v_xor_b32_e32 v3, 0x80000000, v41
	v_xor_b32_e32 v20, 0x80000000, v38
	v_xor_b32_e32 v21, 0x80000000, v39
	v_xor_b32_e32 v22, 0x80000000, v40
	v_and_b32_sdwa v23, v35, v109 dst_sel:DWORD dst_unused:UNUSED_PAD src0_sel:WORD_1 src1_sel:DWORD
	v_and_b32_sdwa v24, v34, v109 dst_sel:DWORD dst_unused:UNUSED_PAD src0_sel:WORD_1 src1_sel:DWORD
	v_and_b32_sdwa v26, v36, v109 dst_sel:DWORD dst_unused:UNUSED_PAD src0_sel:WORD_1 src1_sel:DWORD
	v_and_b32_sdwa v51, v31, v109 dst_sel:DWORD dst_unused:UNUSED_PAD src0_sel:WORD_1 src1_sel:DWORD
	v_add3_u32 v23, v35, v23, s21
	v_add3_u32 v24, v34, v24, s21
	v_and_b32_sdwa v25, v37, v109 dst_sel:DWORD dst_unused:UNUSED_PAD src0_sel:WORD_1 src1_sel:DWORD
	v_add3_u32 v26, v36, v26, s21
	v_bfe_u32 v27, v22, 16, 1
	v_bfe_u32 v28, v21, 16, 1
	v_bfe_u32 v29, v20, 16, 1
	v_bfe_u32 v30, v3, 16, 1
	v_add3_u32 v31, v31, v51, s21
	v_lshrrev_b32_e32 v24, 16, v24
	v_lshrrev_b32_e32 v23, 16, v23
	v_add3_u32 v25, v37, v25, s21
	v_lshrrev_b32_e32 v26, 16, v26
	v_add3_u32 v3, v3, v30, s21
	v_add3_u32 v20, v20, v29, s21
	v_add3_u32 v21, v21, v28, s21
	v_add3_u32 v22, v22, v27, s21
	v_perm_b32 v19, v19, v31, s29
	v_and_or_b32 v22, v22, s28, v26
	v_and_or_b32 v21, v21, s28, v23
	v_and_or_b32 v20, v20, s28, v24
	v_perm_b32 v23, v3, v25, s29
	v_add_u32_e32 v3, s6, v99
	v_lshl_add_u64 v[34:35], v[80:81], 0, s[14:15]
	v_lshl_add_u64 v[36:37], v[84:85], 0, s[14:15]
	s_add_i32 s6, s6, -16
	s_branch .LBB0_1447
.LBB0_1446:
	s_waitcnt vmcnt(0)
.Ls5c_join:
	s_cmpk_eq_i32 s7, 0x81
	s_mov_b32 s8, s7
	v_mov_b64_e32 v[32:33], v[38:39]
	s_cbranch_scc1 .LBB0_1451

; #define LAS __attribute__((address_space(3)))
; __device__ __forceinline__ unsigned cvt_pk_bf16(float lo, float hi) { unsigned r; asm volatile("v_cvt_pk_bf16_f32 %0, %1, %2" : "=v"(r) : "v"(lo), "v"(hi)); return r; }
; __device__ __forceinline__ float gelu_erf_fast(float v) { return 0.5f * v * (1.0f + erf_as(v * 0.70710678118654752f)); }
; #define LDS_WAIT() asm volatile("s_waitcnt lgkmcnt(0)" ::: "memory")
; __device__ __forceinline__ f32x4 unpack4(u32x2 q) { return (f32x4){bflo(q.x), bfhi(q.x), bflo(q.y), bfhi(q.y)}; }
; __device__ __forceinline__ void phase_s5p(const float* const (&in)[34], unsigned char* ws, LAS unsigned char* lds, int G) {
;     ...
;                 LAS unsigned char* XB = XB0 + (ck & 1) * 4352;
;                 const bf16x8 x0 = *(const LAS bf16x8*)(XB + fr * 272 + 0 * 64 + fq * 16), x1 = *(const LAS bf16x8*)(XB + fr * 272 + 1 * 64 + fq * 16);
;                 const bf16x8 x2 = *(const LAS bf16x8*)(XB + fr * 272 + 2 * 64 + fq * 16), x3 = *(const LAS bf16x8*)(XB + fr * 272 + 3 * 64 + fq * 16);
;                 LDS_WAIT();
;                 *(volatile LAS unsigned*)fcons = (unsigned)(base + ck + 1);
;                 f32x4 ya = __builtin_amdgcn_mfma_f32_16x16x32_bf16(cop[0], x0, (f32x4){0.f, 0.f, 0.f, 0.f}, 0, 0, 0), yb = __builtin_amdgcn_mfma_f32_16x16x32_bf16(cop[1], x1, (f32x4){0.f, 0.f, 0.f, 0.f}, 0, 0, 0);
;                 ya = __builtin_amdgcn_mfma_f32_16x16x32_bf16(cop[2], x2, ya, 0, 0, 0); yb = __builtin_amdgcn_mfma_f32_16x16x32_bf16(cop[3], x3, yb, 0, 0, 0);
;                 const int pos = ck * 16 + fr;
;                 f32x4 yv = (ya + yb) + unpack4(usk) * dsk;
;                 yv[0] = gelu_erf_fast(yv[0]); yv[1] = gelu_erf_fast(yv[1]); yv[2] = gelu_erf_fast(yv[2]); yv[3] = gelu_erf_fast(yv[3]);
;                 if (b == 0 || pos >= NMETA) { u32x2 o; o.x = cvt_pk_bf16(yv[0], yv[1]); o.y = cvt_pk_bf16(yv[2], yv[3]); *(u32x2*)(YS + (size_t)rowof(b, pos) * 2048 + g * 16 + 4 * fq) = o; }
;             }
.LBB0_1449:
	s_add_i32 s9, s9, 1
	s_bitcmp1_b32 s8, 0
	s_cselect_b32 s14, 0x1100, 0
	v_add_u32_e32 v44, s14, v83
	ds_read_b128 v[24:27], v44 offset:20992
	ds_read_b128 v[28:31], v44 offset:21056
	ds_read_b128 v[40:43], v44 offset:21120
	ds_read_b128 v[44:47], v44 offset:21184
	s_cmp_eq_u32 s8, 0
	s_waitcnt lgkmcnt(3)
	v_mfma_f32_16x16x32_bf16 v[24:27], v[8:11], v[24:27], 0
	s_waitcnt lgkmcnt(0)
	s_cselect_b64 s[16:17], -1, 0
	s_and_b64 s[16:17], s[4:5], s[16:17]
	s_waitcnt lgkmcnt(2)
	v_mfma_f32_16x16x32_bf16 v[28:31], v[12:15], v[28:31], 0
	v_mov_b32_e32 v48, s18
	s_and_b64 vcc, exec, s[16:17]
	s_waitcnt lgkmcnt(1)
	v_mfma_f32_16x16x32_bf16 v[24:27], v[16:19], v[40:43], v[24:27]
	v_mov_b32_e32 v40, s9
	ds_write_b32 v48, v40 offset:29700
	s_waitcnt lgkmcnt(1)
	v_mfma_f32_16x16x32_bf16 v[28:31], v[20:23], v[44:47], v[28:31]
	s_cbranch_vccnz .LBB0_1446
	s_nop 6
	v_pk_add_f32 v[26:27], v[26:27], v[30:31]
	s_waitcnt vmcnt(1)
	v_lshlrev_b32_e32 v30, 16, v33
	v_and_b32_e32 v31, 0xffff0000, v33
	v_pk_fma_f32 v[26:27], v[6:7], v[30:31], v[26:27]
	v_pk_add_f32 v[24:25], v[24:25], v[28:29]
	v_mul_f32_e32 v30, 0x3f3504f3, v27
	v_fma_f32 v29, |v30|, s30, 1.0
	v_rcp_f32_e32 v31, v29
	v_lshlrev_b32_e32 v28, 16, v32
	v_and_b32_e32 v29, 0xffff0000, v32
	v_pk_fma_f32 v[24:25], v[4:5], v[28:29], v[24:25]
	v_mul_f32_e64 v29, |v30|, s31
	v_fmamk_f32 v28, v31, 0x3f87dc22, v105
	v_mul_f32_e64 v29, |v30|, v29
	v_fmaak_f32 v28, v28, v31, 0x3fb5f0e3
	v_exp_f32_e32 v29, v29
	v_fmaak_f32 v28, v28, v31, 0xbe91a98e
	v_fmaak_f32 v28, v28, v31, 0x3e827906
	v_mul_f32_e64 v28, v28, -v31
	v_fma_f32 v28, v28, v29, 1.0
	v_mul_f32_e32 v29, 0x3f3504f3, v26
	v_bfi_b32 v28, s35, v28, v30
	v_fma_f32 v30, |v29|, s30, 1.0
	v_rcp_f32_e32 v30, v30
	v_mul_f32_e32 v27, 0.5, v27
	v_add_f32_e32 v28, 1.0, v28
	v_mul_f32_e64 v31, |v29|, s31
	v_mul_f32_e32 v27, v27, v28
	v_fmamk_f32 v28, v30, 0x3f87dc22, v105
	v_mul_f32_e64 v31, |v29|, v31
	v_fmaak_f32 v28, v28, v30, 0x3fb5f0e3
	v_exp_f32_e32 v31, v31
	v_fmaak_f32 v28, v28, v30, 0xbe91a98e
	v_fmaak_f32 v28, v28, v30, 0x3e827906
	v_mul_f32_e64 v28, v28, -v30
	v_fma_f32 v28, v28, v31, 1.0
	v_bfi_b32 v28, s35, v28, v29
	v_mul_f32_e32 v29, 0x3f3504f3, v25
	v_fma_f32 v30, |v29|, s30, 1.0
	v_rcp_f32_e32 v30, v30
	v_mul_f32_e32 v26, 0.5, v26
	v_add_f32_e32 v28, 1.0, v28
	v_mul_f32_e64 v31, |v29|, s31
	v_mul_f32_e32 v26, v26, v28
	v_fmamk_f32 v28, v30, 0x3f87dc22, v105
	v_mul_f32_e64 v31, |v29|, v31
	v_fmaak_f32 v28, v28, v30, 0x3fb5f0e3
	v_exp_f32_e32 v31, v31
	v_fmaak_f32 v28, v28, v30, 0xbe91a98e
	v_fmaak_f32 v28, v28, v30, 0x3e827906
	v_mul_f32_e64 v28, v28, -v30
	v_fma_f32 v28, v28, v31, 1.0
	v_bfi_b32 v28, s35, v28, v29
	v_mul_f32_e32 v29, 0x3f3504f3, v24
	v_fma_f32 v30, |v29|, s30, 1.0
	v_rcp_f32_e32 v30, v30
	v_mul_f32_e32 v25, 0.5, v25
	v_add_f32_e32 v28, 1.0, v28
	v_mul_f32_e64 v31, |v29|, s31
	v_mul_f32_e32 v25, v25, v28
	v_fmamk_f32 v28, v30, 0x3f87dc22, v105
	v_mul_f32_e64 v31, |v29|, v31
	v_fmaak_f32 v28, v28, v30, 0x3fb5f0e3
	v_exp_f32_e32 v31, v31
	v_fmaak_f32 v28, v28, v30, 0xbe91a98e
	v_fmaak_f32 v28, v28, v30, 0x3e827906
	v_mul_f32_e64 v28, v28, -v30
	v_fma_f32 v28, v28, v31, 1.0
	v_bfi_b32 v28, s35, v28, v29
	v_mul_f32_e32 v24, 0.5, v24
	v_add_f32_e32 v28, 1.0, v28
	v_mul_f32_e32 v24, v24, v28
	v_lshl_or_b32 v28, s8, 4, v98
	s_cmp_eq_u32 s8, 0
	v_cvt_pk_bf16_f32 v24, v24, v25
	v_cvt_pk_bf16_f32 v25, v26, v27
	v_or_b32_e32 v26, 0x2000, v28
	v_add_u32_e32 v27, s6, v28
	s_cselect_b64 vcc, -1, 0
	v_cndmask_b32_e32 v26, v27, v26, vcc
	v_ashrrev_i32_e32 v27, 31, v26
	v_lshlrev_b64 v[26:27], 12, v[26:27]
	v_lshl_add_u64 v[26:27], v[36:37], 0, v[26:27]
	global_store_dwordx2 v[26:27], v[24:25], off
	s_waitcnt vmcnt(1)
	s_branch .Ls5c_join

; #define LAS __attribute__((address_space(3)))
; #define LDS_WAIT() asm volatile("s_waitcnt lgkmcnt(0)" ::: "memory")
; __device__ __forceinline__ void phase_s5p(const float* const (&in)[34], unsigned char* ws, LAS unsigned char* lds, int G) {
;     ...
;             {   const bf16_t* ur0 = U + (size_t)rowof(b, fr) * 2048 + g * 16; u32x4 uz0 = {0u, 0u, 0u, 0u}; if (fq < 2) uz0 = *(const u32x4*)(ur0 + fq * 8);
;                 const bf16_t* ur1 = U + (size_t)rowof(b, 16 + fr) * 2048 + g * 16; if (fq < 2) uz1 = *(const u32x4*)(ur1 + fq * 8);
;                 const bf16x8 uop = __builtin_bit_cast(bf16x8, uz0);
; #pragma unroll
;                 for (int nt = 0; nt < 8; ++nt) { const f32x4 acc = __builtin_amdgcn_mfma_f32_16x16x32_bf16(uop, bop[nt], (f32x4){0.f, 0.f, 0.f, 0.f}, 0, 0, 0);
; #pragma unroll
;                     for (int i = 0; i < 4; ++i) BU0[(4 * fq + i) * 132 + nt * 16 + fr] = acc[i]; }
;                 LDS_WAIT();
;             }
; #pragma unroll 1
;             for (int ck = 0; ck < NCK; ++ck) {
;                 LAS float* BUc = BU0 + (ck & 1) * (16 * 132); LAS float* BUn = BU0 + ((ck + 1) & 1) * (16 * 132); LAS unsigned char* XB = XB0 + (ck & 1) * 4352;
;                 { const int pc = ck + 2 < NCK ? ck + 2 : ck; const bf16_t* ur = U + (size_t)rowof(b, pc * 16 + fr) * 2048 + g * 16; if (fq < 2) uz2 = *(const u32x4*)(ur + fq * 8); }
;     ...
;                 LDS_WAIT();
;                 *(volatile LAS unsigned*)fprod = (unsigned)(base + ck + 1);
;                 uz1 = uz2;
.LBB0_1477:
	s_or_b64 exec, exec, s[4:5]
	s_waitcnt vmcnt(0) lgkmcnt(0)
	v_mfma_f32_16x16x32_bf16 v[48:51], v[42:45], v[10:13], 0
	v_add_u32_e32 v64, 0x1000, v103
	v_add_u32_e32 v65, 0x1400, v103
	v_mul_f32_e32 v93, v46, v47
	v_mfma_f32_16x16x32_bf16 v[52:55], v[42:45], v[6:9], 0
	s_lshl_b32 s14, s7, 1
	s_mov_b32 s8, 0
	s_add_i32 s6, s6, -16
	v_mfma_f32_16x16x32_bf16 v[56:59], v[42:45], v[18:21], 0
	v_lshl_add_u64 v[96:97], v[88:89], 0, s[14:15]
	s_nop 2
	ds_write2_b32 v64, v48, v52 offset1:16
	ds_write2_b32 v64, v49, v53 offset0:132 offset1:148
	v_mfma_f32_16x16x32_bf16 v[60:63], v[42:45], v[14:17], 0
	ds_write2_b32 v65, v50, v54 offset0:8 offset1:24
	ds_write2_b32 v65, v51, v55 offset0:140 offset1:156
	s_nop 5
	ds_write2_b32 v64, v56, v60 offset0:32 offset1:48
	ds_write2_b32 v64, v57, v61 offset0:164 offset1:180
	v_mfma_f32_16x16x32_bf16 v[46:49], v[42:45], v[26:29], 0
	s_add_i32 s7, s63, -1
	v_mov_b32_e32 v94, 0
	v_mov_b32_e32 v114, 0
	v_mfma_f32_16x16x32_bf16 v[50:53], v[42:45], v[22:25], 0
	ds_write2_b32 v65, v58, v62 offset0:40 offset1:56
	ds_write2_b32 v65, v59, v63 offset0:172 offset1:188
	s_nop 5
	ds_write2_b32 v64, v46, v50 offset0:64 offset1:80
	ds_write2_b32 v64, v47, v51 offset0:196 offset1:212
	ds_write2_b32 v65, v48, v52 offset0:72 offset1:88
	ds_write2_b32 v65, v49, v53 offset0:204 offset1:220
	v_mfma_f32_16x16x32_bf16 v[54:57], v[42:45], v[34:37], 0
	v_mfma_f32_16x16x32_bf16 v[42:45], v[42:45], v[30:33], 0
	s_nop 7
	ds_write2_b32 v64, v54, v42 offset0:96 offset1:112
	ds_write2_b32 v64, v55, v43 offset0:228 offset1:244
	ds_write2_b32 v65, v56, v44 offset0:104 offset1:120
	ds_write2_b32 v65, v57, v45 offset0:236 offset1:252
	s_waitcnt lgkmcnt(0)
	v_mov_b64_e32 v[44:45], v[4:5]
	v_mov_b64_e32 v[42:43], v[2:3]
	v_mov_b32_e32 v120, 0
	v_mov_b32_e32 v121, 0
	v_mov_b32_e32 v122, 0
	v_mov_b32_e32 v123, 0
	s_and_saveexec_b64 s[4:5], s[0:1]
	v_or_b32_e32 v3, 32, v98
	v_add_u32_e32 v4, s6, v3
	v_ashrrev_i32_e32 v5, 31, v4
	v_lshlrev_b64 v[4:5], 12, v[4:5]
	v_lshl_add_u64 v[4:5], v[96:97], 0, v[4:5]
	global_load_dwordx4 v[42:45], v[4:5], off
	s_or_b64 exec, exec, s[4:5]
	s_branch .LBB0_1479
.LBB0_1478:
	s_waitcnt lgkmcnt(0)
	s_add_i32 s5, s4, s63
	s_waitcnt vmcnt(1)
	s_nop 2
	s_bitcmp1_b32 s8, 0
	s_cbranch_scc1 .Ls5p_cpB
	v_mov_b64_e32 v[38:39], v[42:43]
	v_mov_b64_e32 v[40:41], v[44:45]
	s_branch .Ls5p_cpdone
.Ls5p_cpB:
	v_mov_b64_e32 v[38:39], v[120:121]
	v_mov_b64_e32 v[40:41], v[122:123]
.Ls5p_cpdone:
	v_mov_b32_e32 v3, s18
	v_mov_b32_e32 v4, s5
	s_cmpk_eq_i32 s4, 0x81
	s_mov_b32 s8, s4
	ds_write_b32 v3, v4 offset:29696
	s_cbranch_scc1 .LBB0_1443
.LBB0_1479:
	s_and_saveexec_b64 s[4:5], s[0:1]
	s_cbranch_execz .LBB0_1481
	s_lshl_b32 s9, s8, 4
	s_add_i32 s14, s9, 48
	s_cmpk_lt_u32 s8, 0x7e
	s_cselect_b32 s9, s14, s9
	s_cmp_eq_u32 s9, 0
	v_or_b32_e32 v3, s9, v98
	v_or_b32_e32 v4, 0x2000, v3
	v_add_u32_e32 v3, s6, v3
	s_cselect_b64 vcc, -1, 0
	v_cndmask_b32_e32 v4, v3, v4, vcc
	v_ashrrev_i32_e32 v5, 31, v4
	v_lshlrev_b64 v[4:5], 12, v[4:5]
	v_lshl_add_u64 v[4:5], v[96:97], 0, v[4:5]
	s_bitcmp1_b32 s8, 0
	s_cbranch_scc1 .Ls5p_odd
	global_load_dwordx4 v[120:123], v[4:5], off
	s_branch .LBB0_1481
.Ls5p_odd:
	global_load_dwordx4 v[42:45], v[4:5], off
